# MoBA tile loops: counted lgkmcnt(6) waits before the 1st and 5th QK^T MFMA instead of lgkmcnt(0) before the 1st
# baseline (speedup 1.0000x reference)
.Lmoba0_a:
	v_and_b32_e32 v33, s6, v198
	v_cmp_ne_u32_e32 vcc, 0, v33
	v_fma_f32 v32, v137, v32, -v197
	s_or_b64 vcc, s[0:1], vcc
	v_cndmask_b32_e32 v32, v192, v32, vcc
	v_pk_add_f32 v[48:49], v[136:137], v[32:33] op_sel_hi:[1,0]
	v_pk_add_f32 v[50:51], v[142:143], v[32:33] op_sel_hi:[1,0]
	v_pk_add_f32 v[52:53], v[144:145], v[32:33] op_sel_hi:[1,0]
	v_pk_add_f32 v[54:55], v[146:147], v[32:33] op_sel_hi:[1,0]
	v_pk_add_f32 v[56:57], v[148:149], v[32:33] op_sel_hi:[1,0]
	v_pk_add_f32 v[58:59], v[150:151], v[32:33] op_sel_hi:[1,0]
	v_pk_add_f32 v[60:61], v[152:153], v[32:33] op_sel_hi:[1,0]
	v_pk_add_f32 v[62:63], v[154:155], v[32:33] op_sel_hi:[1,0]
	v_mov_b32_e32 v139, v138
	v_pk_add_f32 v[46:47], v[138:139], v[62:63]
	v_pk_add_f32 v[44:45], v[138:139], v[60:61]
	v_pk_add_f32 v[42:43], v[138:139], v[58:59]
	v_pk_add_f32 v[40:41], v[138:139], v[56:57]
	v_pk_add_f32 v[38:39], v[138:139], v[54:55]
	v_pk_add_f32 v[36:37], v[138:139], v[52:53]
	v_pk_add_f32 v[34:35], v[138:139], v[50:51]
	v_pk_add_f32 v[32:33], v[140:141], v[48:49]
	v_add_u32_e32 v139, s33, v166
	ds_read_b64_tr_b16 v[100:101], v139 offset:24576
	ds_read_b64_tr_b16 v[102:103], v139 offset:25088
	ds_read_b64_tr_b16 v[92:93], v139 offset:25600
	ds_read_b64_tr_b16 v[94:95], v139 offset:26112
	ds_read_b128 v[104:107], v160 offset:4096
	ds_read_b128 v[108:111], v160 offset:4608
	s_waitcnt lgkmcnt(6)
	v_mfma_f32_32x32x16_bf16 v[48:63], v[80:83], v[76:79], v[48:63]
	v_mfma_f32_32x32x16_bf16 v[32:47], v[84:87], v[76:79], v[32:47]
	ds_read_b64_tr_b16 v[84:85], v139 offset:26624
	ds_read_b64_tr_b16 v[86:87], v139 offset:27136
	ds_read_b64_tr_b16 v[80:81], v139 offset:27648
	ds_read_b64_tr_b16 v[82:83], v139 offset:28160
	ds_read_b128 v[202:205], v160 offset:6144
	ds_read_b128 v[206:209], v160 offset:6656
	v_mfma_f32_32x32x16_bf16 v[48:63], v[88:91], v[72:75], v[48:63]
	v_mfma_f32_32x32x16_bf16 v[32:47], v[96:99], v[72:75], v[32:47]
	s_waitcnt lgkmcnt(6)
	v_mfma_f32_32x32x16_bf16 v[48:63], v[104:107], v[68:71], v[48:63]
	v_mfma_f32_32x32x16_bf16 v[32:47], v[108:111], v[68:71], v[32:47]
	s_waitcnt lgkmcnt(0)
	v_mfma_f32_32x32x16_bf16 v[48:63], v[202:205], v[64:67], v[48:63]
	ds_read_b64_tr_b16 v[108:109], v139 offset:28672
	ds_read_b64_tr_b16 v[110:111], v139 offset:29184
	ds_read_b64_tr_b16 v[104:105], v139 offset:29696
	ds_read_b64_tr_b16 v[106:107], v139 offset:30208
	v_mfma_f32_32x32x16_bf16 v[32:47], v[206:209], v[64:67], v[32:47]
	ds_read_b64_tr_b16 v[96:97], v139 offset:30720
	ds_read_b64_tr_b16 v[98:99], v139 offset:31232
	ds_read_b64_tr_b16 v[88:89], v139 offset:31744
	ds_read_b64_tr_b16 v[90:91], v139 offset:32256
	s_add_i32 s6, s56, 63
	s_cmp_gt_u32 s6, s8
	s_cselect_b64 s[6:7], -1, 0
	s_and_b64 s[0:1], s[0:1], s[6:7]
	s_andn2_b64 vcc, exec, s[0:1]
	s_cbranch_vccnz .LBB0_496
	v_add_u32_e32 v139, 27, v200
	v_cmp_lt_i32_e32 vcc, -1, v139
	s_nop 1
	v_cndmask_b32_e32 v48, v192, v48, vcc
	v_cmp_lt_i32_e32 vcc, 31, v139
	v_add_u32_e32 v139, 26, v200
	s_nop 0
	v_cndmask_b32_e32 v32, v192, v32, vcc
	v_cmp_lt_i32_e32 vcc, -1, v139
	s_nop 1
	v_cndmask_b32_e32 v49, v192, v49, vcc
	v_cmp_lt_i32_e32 vcc, 31, v139
	v_add_u32_e32 v139, 25, v200
	s_nop 0
	v_cndmask_b32_e32 v33, v192, v33, vcc
	v_cmp_lt_i32_e32 vcc, -1, v139
	s_nop 1
	v_cndmask_b32_e32 v50, v192, v50, vcc
	v_cmp_lt_i32_e32 vcc, 31, v139
	v_add_u32_e32 v139, 24, v200
	s_nop 0
	v_cndmask_b32_e32 v34, v192, v34, vcc
	v_cmp_lt_i32_e32 vcc, -1, v139
	s_nop 1
	v_cndmask_b32_e32 v51, v192, v51, vcc
	v_cmp_lt_i32_e32 vcc, 31, v139
	v_add_u32_e32 v139, 19, v200
	s_nop 0
	v_cndmask_b32_e32 v35, v192, v35, vcc
	v_cmp_lt_i32_e32 vcc, -1, v139
	s_nop 1
	v_cndmask_b32_e32 v52, v192, v52, vcc
	v_cmp_lt_i32_e32 vcc, 31, v139
	v_add_u32_e32 v139, 18, v200
	s_nop 0
	v_cndmask_b32_e32 v36, v192, v36, vcc
	v_cmp_lt_i32_e32 vcc, -1, v139
	s_nop 1
	v_cndmask_b32_e32 v53, v192, v53, vcc
	v_cmp_lt_i32_e32 vcc, 31, v139
	v_add_u32_e32 v139, 17, v200
	s_nop 0
	v_cndmask_b32_e32 v37, v192, v37, vcc
	v_cmp_lt_i32_e32 vcc, -1, v139
	s_nop 1
	v_cndmask_b32_e32 v54, v192, v54, vcc
	v_cmp_lt_i32_e32 vcc, 31, v139
	v_add_u32_e32 v139, 16, v200
	s_nop 0
	v_cndmask_b32_e32 v38, v192, v38, vcc
	v_cmp_lt_i32_e32 vcc, -1, v139
	s_nop 1
	v_cndmask_b32_e32 v55, v192, v55, vcc
	v_cmp_lt_i32_e32 vcc, 31, v139
	v_add_u32_e32 v139, 11, v200
	s_nop 0
	v_cndmask_b32_e32 v39, v192, v39, vcc
	v_cmp_lt_i32_e32 vcc, -1, v139
	s_nop 1
	v_cndmask_b32_e32 v56, v192, v56, vcc
	v_cmp_lt_i32_e32 vcc, 31, v139
	v_add_u32_e32 v139, 10, v200
	s_nop 0
	v_cndmask_b32_e32 v40, v192, v40, vcc
	v_cmp_lt_i32_e32 vcc, -1, v139
	s_nop 1
	v_cndmask_b32_e32 v57, v192, v57, vcc
	v_cmp_lt_i32_e32 vcc, 31, v139
	v_add_u32_e32 v139, 9, v200
	s_nop 0
	v_cndmask_b32_e32 v41, v192, v41, vcc
	v_cmp_lt_i32_e32 vcc, -1, v139
	s_nop 1
	v_cndmask_b32_e32 v58, v192, v58, vcc
	v_cmp_lt_i32_e32 vcc, 31, v139
	v_add_u32_e32 v139, 8, v200
	s_nop 0
	v_cndmask_b32_e32 v42, v192, v42, vcc
	v_cmp_lt_i32_e32 vcc, -1, v139
	s_nop 1
	v_cndmask_b32_e32 v59, v192, v59, vcc
	v_cmp_lt_i32_e32 vcc, 31, v139
	v_add_u32_e32 v139, 3, v200
	s_nop 0
	v_cndmask_b32_e32 v43, v192, v43, vcc
	v_cmp_lt_i32_e32 vcc, -1, v139
	s_nop 1
	v_cndmask_b32_e32 v60, v192, v60, vcc
	v_cmp_lt_i32_e32 vcc, 31, v139
	v_add_u32_e32 v139, 2, v200
	s_nop 0
	v_cndmask_b32_e32 v44, v192, v44, vcc
	v_cmp_lt_i32_e32 vcc, -1, v139
	s_nop 1
	v_cndmask_b32_e32 v61, v192, v61, vcc
	v_cmp_lt_i32_e32 vcc, 31, v139
	v_add_u32_e32 v139, 1, v200
	s_nop 0
	v_cndmask_b32_e32 v45, v192, v45, vcc
	v_cmp_lt_i32_e32 vcc, -1, v139
	s_nop 1
	v_cndmask_b32_e32 v62, v192, v62, vcc
	v_cmp_lt_i32_e32 vcc, 31, v139
	s_nop 1
	v_cndmask_b32_e32 v46, v192, v46, vcc
	v_cmp_lt_i32_e32 vcc, -1, v200
	s_nop 1
	v_cndmask_b32_e32 v63, v192, v63, vcc
	v_cmp_lt_i32_e32 vcc, 31, v200
	s_nop 1
	v_cndmask_b32_e32 v47, v192, v47, vcc

.Lmoba1_a:
	v_and_b32_e32 v33, s6, v198
	v_cmp_ne_u32_e32 vcc, 0, v33
	v_fma_f32 v32, v137, v32, -v197
	s_or_b64 vcc, s[0:1], vcc
	v_cndmask_b32_e32 v32, v192, v32, vcc
	v_pk_add_f32 v[48:49], v[136:137], v[32:33] op_sel_hi:[1,0]
	v_pk_add_f32 v[50:51], v[142:143], v[32:33] op_sel_hi:[1,0]
	v_pk_add_f32 v[52:53], v[144:145], v[32:33] op_sel_hi:[1,0]
	v_pk_add_f32 v[54:55], v[146:147], v[32:33] op_sel_hi:[1,0]
	v_pk_add_f32 v[56:57], v[148:149], v[32:33] op_sel_hi:[1,0]
	v_pk_add_f32 v[58:59], v[150:151], v[32:33] op_sel_hi:[1,0]
	v_pk_add_f32 v[60:61], v[152:153], v[32:33] op_sel_hi:[1,0]
	v_pk_add_f32 v[62:63], v[154:155], v[32:33] op_sel_hi:[1,0]
	v_mov_b32_e32 v139, v138
	v_pk_add_f32 v[46:47], v[138:139], v[62:63]
	v_pk_add_f32 v[44:45], v[138:139], v[60:61]
	v_pk_add_f32 v[42:43], v[138:139], v[58:59]
	v_pk_add_f32 v[40:41], v[138:139], v[56:57]
	v_pk_add_f32 v[38:39], v[138:139], v[54:55]
	v_pk_add_f32 v[36:37], v[138:139], v[52:53]
	v_pk_add_f32 v[34:35], v[138:139], v[50:51]
	v_pk_add_f32 v[32:33], v[140:141], v[48:49]
	v_add_u32_e32 v139, s36, v166
	ds_read_b64_tr_b16 v[100:101], v139 offset:24576
	ds_read_b64_tr_b16 v[102:103], v139 offset:25088
	ds_read_b64_tr_b16 v[92:93], v139 offset:25600
	ds_read_b64_tr_b16 v[94:95], v139 offset:26112
	ds_read_b128 v[108:111], v160 offset:4096
	ds_read_b128 v[202:205], v160 offset:4608
	s_waitcnt lgkmcnt(6)
	v_mfma_f32_32x32x16_bf16 v[48:63], v[80:83], v[76:79], v[48:63]
	ds_read_b64_tr_b16 v[84:85], v139 offset:26624
	ds_read_b64_tr_b16 v[86:87], v139 offset:27136
	ds_read_b64_tr_b16 v[80:81], v139 offset:27648
	ds_read_b64_tr_b16 v[82:83], v139 offset:28160
	ds_read_b128 v[206:209], v160 offset:6144
	ds_read_b128 v[210:213], v160 offset:6656
	v_mfma_f32_32x32x16_bf16 v[32:47], v[88:91], v[76:79], v[32:47]
	v_mfma_f32_32x32x16_bf16 v[48:63], v[96:99], v[72:75], v[48:63]
	v_mfma_f32_32x32x16_bf16 v[32:47], v[104:107], v[72:75], v[32:47]
	s_waitcnt lgkmcnt(6)
	v_mfma_f32_32x32x16_bf16 v[48:63], v[108:111], v[68:71], v[48:63]
	v_mfma_f32_32x32x16_bf16 v[32:47], v[202:205], v[68:71], v[32:47]
	s_waitcnt lgkmcnt(0)
	v_mfma_f32_32x32x16_bf16 v[48:63], v[206:209], v[64:67], v[48:63]
	ds_read_b64_tr_b16 v[108:109], v139 offset:28672
	ds_read_b64_tr_b16 v[110:111], v139 offset:29184
	ds_read_b64_tr_b16 v[104:105], v139 offset:29696
	ds_read_b64_tr_b16 v[106:107], v139 offset:30208
	v_mfma_f32_32x32x16_bf16 v[32:47], v[210:213], v[64:67], v[32:47]
	ds_read_b64_tr_b16 v[96:97], v139 offset:30720
	ds_read_b64_tr_b16 v[98:99], v139 offset:31232
	ds_read_b64_tr_b16 v[88:89], v139 offset:31744
	ds_read_b64_tr_b16 v[90:91], v139 offset:32256
	s_add_i32 s6, s56, 63
	s_cmp_gt_u32 s6, s8
	s_cselect_b64 s[6:7], -1, 0
	s_and_b64 s[0:1], s[0:1], s[6:7]
	s_andn2_b64 vcc, exec, s[0:1]
	s_cbranch_vccnz .LBB0_3035
	v_add_u32_e32 v139, 27, v200
	v_cmp_lt_i32_e32 vcc, -1, v139
	s_nop 1
	v_cndmask_b32_e32 v48, v192, v48, vcc
	v_cmp_lt_i32_e32 vcc, 31, v139
	v_add_u32_e32 v139, 26, v200
	s_nop 0
	v_cndmask_b32_e32 v32, v192, v32, vcc
	v_cmp_lt_i32_e32 vcc, -1, v139
	s_nop 1
	v_cndmask_b32_e32 v49, v192, v49, vcc
	v_cmp_lt_i32_e32 vcc, 31, v139
	v_add_u32_e32 v139, 25, v200
	s_nop 0
	v_cndmask_b32_e32 v33, v192, v33, vcc
	v_cmp_lt_i32_e32 vcc, -1, v139
	s_nop 1
	v_cndmask_b32_e32 v50, v192, v50, vcc
	v_cmp_lt_i32_e32 vcc, 31, v139
	v_add_u32_e32 v139, 24, v200
	s_nop 0
	v_cndmask_b32_e32 v34, v192, v34, vcc
	v_cmp_lt_i32_e32 vcc, -1, v139
	s_nop 1
	v_cndmask_b32_e32 v51, v192, v51, vcc
	v_cmp_lt_i32_e32 vcc, 31, v139
	v_add_u32_e32 v139, 19, v200
	s_nop 0
	v_cndmask_b32_e32 v35, v192, v35, vcc
	v_cmp_lt_i32_e32 vcc, -1, v139
	s_nop 1
	v_cndmask_b32_e32 v52, v192, v52, vcc
	v_cmp_lt_i32_e32 vcc, 31, v139
	v_add_u32_e32 v139, 18, v200
	s_nop 0
	v_cndmask_b32_e32 v36, v192, v36, vcc
	v_cmp_lt_i32_e32 vcc, -1, v139
	s_nop 1
	v_cndmask_b32_e32 v53, v192, v53, vcc
	v_cmp_lt_i32_e32 vcc, 31, v139
	v_add_u32_e32 v139, 17, v200
	s_nop 0
	v_cndmask_b32_e32 v37, v192, v37, vcc
	v_cmp_lt_i32_e32 vcc, -1, v139
	s_nop 1
	v_cndmask_b32_e32 v54, v192, v54, vcc
	v_cmp_lt_i32_e32 vcc, 31, v139
	v_add_u32_e32 v139, 16, v200
	s_nop 0
	v_cndmask_b32_e32 v38, v192, v38, vcc
	v_cmp_lt_i32_e32 vcc, -1, v139
	s_nop 1
	v_cndmask_b32_e32 v55, v192, v55, vcc
	v_cmp_lt_i32_e32 vcc, 31, v139
	v_add_u32_e32 v139, 11, v200
	s_nop 0
	v_cndmask_b32_e32 v39, v192, v39, vcc
	v_cmp_lt_i32_e32 vcc, -1, v139
	s_nop 1
	v_cndmask_b32_e32 v56, v192, v56, vcc
	v_cmp_lt_i32_e32 vcc, 31, v139
	v_add_u32_e32 v139, 10, v200
	s_nop 0
	v_cndmask_b32_e32 v40, v192, v40, vcc
	v_cmp_lt_i32_e32 vcc, -1, v139
	s_nop 1
	v_cndmask_b32_e32 v57, v192, v57, vcc
	v_cmp_lt_i32_e32 vcc, 31, v139
	v_add_u32_e32 v139, 9, v200
	s_nop 0
	v_cndmask_b32_e32 v41, v192, v41, vcc
	v_cmp_lt_i32_e32 vcc, -1, v139
	s_nop 1
	v_cndmask_b32_e32 v58, v192, v58, vcc
	v_cmp_lt_i32_e32 vcc, 31, v139
	v_add_u32_e32 v139, 8, v200
	s_nop 0
	v_cndmask_b32_e32 v42, v192, v42, vcc
	v_cmp_lt_i32_e32 vcc, -1, v139
	s_nop 1
	v_cndmask_b32_e32 v59, v192, v59, vcc
	v_cmp_lt_i32_e32 vcc, 31, v139
	v_add_u32_e32 v139, 3, v200
	s_nop 0
	v_cndmask_b32_e32 v43, v192, v43, vcc
	v_cmp_lt_i32_e32 vcc, -1, v139
	s_nop 1
	v_cndmask_b32_e32 v60, v192, v60, vcc
	v_cmp_lt_i32_e32 vcc, 31, v139
	v_add_u32_e32 v139, 2, v200
	s_nop 0
	v_cndmask_b32_e32 v44, v192, v44, vcc
	v_cmp_lt_i32_e32 vcc, -1, v139
	s_nop 1
	v_cndmask_b32_e32 v61, v192, v61, vcc
	v_cmp_lt_i32_e32 vcc, 31, v139
	v_add_u32_e32 v139, 1, v200
	s_nop 0
	v_cndmask_b32_e32 v45, v192, v45, vcc
	v_cmp_lt_i32_e32 vcc, -1, v139
	s_nop 1
	v_cndmask_b32_e32 v62, v192, v62, vcc
	v_cmp_lt_i32_e32 vcc, 31, v139
	s_nop 1
	v_cndmask_b32_e32 v46, v192, v46, vcc
	v_cmp_lt_i32_e32 vcc, -1, v200
	s_nop 1
	v_cndmask_b32_e32 v63, v192, v63, vcc
	v_cmp_lt_i32_e32 vcc, 31, v200
	s_nop 1
	v_cndmask_b32_e32 v47, v192, v47, vcc
